# gemm: front-loaded memory phase - LDS-DMA slots 0,3,6 in both blocks (all DMAs and reads in the first 9 gaps, 9-MFMA pure-compute tail before each wait/barrier), on top of the balanced read split
# speedup vs baseline: 1.0053x; 1.0044x over previous
.Lgemm_T_loop:
	s_waitcnt lgkmcnt(0)
	s_add_u32 m0, s11, 0x1e080
	ds_read_b128 v[146:149], v164
	global_load_lds_dwordx4 v[220:221], off offset:-128
	v_mfma_f32_16x16x32_f16 v[82:85], v[134:137], v[86:89], v[82:85]
	ds_read_b128 v[150:153], v164 offset:2048
	v_mfma_f32_16x16x32_f16 v[58:61], v[138:141], v[86:89], v[58:61]
	ds_read_b128 v[154:157], v164 offset:4096
	v_mfma_f32_16x16x32_f16 v[14:17], v[142:145], v[86:89], v[14:17]
	s_add_u32 m0, s11, 0x20080
	ds_read_b128 v[110:113], v160
	global_load_lds_dwordx4 v[224:225], off offset:-128
	v_mfma_f32_16x16x32_f16 v[78:81], v[134:137], v[90:93], v[78:81]
	ds_read_b128 v[114:117], v160 offset:2048
	v_mfma_f32_16x16x32_f16 v[22:25], v[138:141], v[90:93], v[22:25]
	ds_read_b128 v[118:121], v160 offset:4096
	v_mfma_f32_16x16x32_f16 v[30:33], v[142:145], v[90:93], v[30:33]
	s_add_u32 m0, s11, 0x22080
	ds_read_b128 v[122:125], v160 offset:6144
	global_load_lds_dwordx4 v[228:229], off offset:-128
	v_mfma_f32_16x16x32_f16 v[74:77], v[134:137], v[94:97], v[74:77]
	ds_read_b128 v[126:129], v160 offset:8192
	v_mfma_f32_16x16x32_f16 v[18:21], v[138:141], v[94:97], v[18:21]
	ds_read_b128 v[130:133], v160 offset:10240
	v_mfma_f32_16x16x32_f16 v[26:29], v[142:145], v[94:97], v[26:29]
	v_mfma_f32_16x16x32_f16 v[70:73], v[134:137], v[98:101], v[70:73]
	v_mfma_f32_16x16x32_f16 v[46:49], v[138:141], v[98:101], v[46:49]
	v_mfma_f32_16x16x32_f16 v[240:243], v[142:145], v[98:101], v[240:243]
	v_mfma_f32_16x16x32_f16 v[66:69], v[134:137], v[102:105], v[66:69]
	v_mfma_f32_16x16x32_f16 v[42:45], v[138:141], v[102:105], v[42:45]
	v_mfma_f32_16x16x32_f16 v[236:239], v[142:145], v[102:105], v[236:239]
	v_mfma_f32_16x16x32_f16 v[62:65], v[134:137], v[106:109], v[62:65]
	v_mfma_f32_16x16x32_f16 v[38:41], v[138:141], v[106:109], v[38:41]
	v_mfma_f32_16x16x32_f16 v[34:37], v[142:145], v[106:109], v[34:37]
	s_waitcnt vmcnt(6) lgkmcnt(0)
	s_barrier
	s_add_u32 m0, s11, 0x0
	ds_read_b128 v[134:137], v162 offset:49152
	global_load_lds_dwordx4 v[218:219], off
	v_mfma_f32_16x16x32_f16 v[82:85], v[146:149], v[110:113], v[82:85]
	ds_read_b128 v[138:141], v162 offset:51200
	v_mfma_f32_16x16x32_f16 v[58:61], v[150:153], v[110:113], v[58:61]
	ds_read_b128 v[142:145], v162 offset:53248
	v_mfma_f32_16x16x32_f16 v[14:17], v[154:157], v[110:113], v[14:17]
	s_add_u32 m0, s11, 0x2000
	ds_read_b128 v[86:89], v158 offset:49152
	global_load_lds_dwordx4 v[222:223], off
	v_mfma_f32_16x16x32_f16 v[78:81], v[146:149], v[114:117], v[78:81]
	ds_read_b128 v[90:93], v158 offset:51200
	v_mfma_f32_16x16x32_f16 v[22:25], v[150:153], v[114:117], v[22:25]
	ds_read_b128 v[94:97], v158 offset:53248
	v_mfma_f32_16x16x32_f16 v[30:33], v[154:157], v[114:117], v[30:33]
	s_add_u32 m0, s11, 0x4000
	ds_read_b128 v[98:101], v158 offset:55296
	global_load_lds_dwordx4 v[226:227], off
	v_mfma_f32_16x16x32_f16 v[74:77], v[146:149], v[118:121], v[74:77]
	ds_read_b128 v[102:105], v158 offset:57344
	v_mfma_f32_16x16x32_f16 v[18:21], v[150:153], v[118:121], v[18:21]
	ds_read_b128 v[106:109], v158 offset:59392
	v_mfma_f32_16x16x32_f16 v[26:29], v[154:157], v[118:121], v[26:29]
	v_mfma_f32_16x16x32_f16 v[70:73], v[146:149], v[122:125], v[70:73]
	v_mfma_f32_16x16x32_f16 v[46:49], v[150:153], v[122:125], v[46:49]
	v_mfma_f32_16x16x32_f16 v[240:243], v[154:157], v[122:125], v[240:243]
	v_mfma_f32_16x16x32_f16 v[66:69], v[146:149], v[126:129], v[66:69]
	v_mfma_f32_16x16x32_f16 v[42:45], v[150:153], v[126:129], v[42:45]
	v_mfma_f32_16x16x32_f16 v[236:239], v[154:157], v[126:129], v[236:239]
	v_mfma_f32_16x16x32_f16 v[62:65], v[146:149], v[130:133], v[62:65]
	v_mfma_f32_16x16x32_f16 v[38:41], v[150:153], v[130:133], v[38:41]
	v_mfma_f32_16x16x32_f16 v[34:37], v[154:157], v[130:133], v[34:37]
	s_waitcnt lgkmcnt(0)
	s_add_u32 m0, s11, 0x6000
	ds_read_b128 v[146:149], v164 offset:49152
	global_load_lds_dwordx4 v[220:221], off
	v_mfma_f32_16x16x32_f16 v[82:85], v[134:137], v[86:89], v[82:85]
	ds_read_b128 v[150:153], v164 offset:51200
	v_mfma_f32_16x16x32_f16 v[58:61], v[138:141], v[86:89], v[58:61]
	ds_read_b128 v[154:157], v164 offset:53248
	v_mfma_f32_16x16x32_f16 v[14:17], v[142:145], v[86:89], v[14:17]
	s_add_u32 m0, s11, 0x8000
	ds_read_b128 v[110:113], v160 offset:49152
	global_load_lds_dwordx4 v[224:225], off
	v_mfma_f32_16x16x32_f16 v[78:81], v[134:137], v[90:93], v[78:81]
	ds_read_b128 v[114:117], v160 offset:51200
	v_mfma_f32_16x16x32_f16 v[22:25], v[138:141], v[90:93], v[22:25]
	ds_read_b128 v[118:121], v160 offset:53248
	v_mfma_f32_16x16x32_f16 v[30:33], v[142:145], v[90:93], v[30:33]
	s_add_u32 m0, s11, 0xa000
	ds_read_b128 v[122:125], v160 offset:55296
	global_load_lds_dwordx4 v[228:229], off
	v_mfma_f32_16x16x32_f16 v[74:77], v[134:137], v[94:97], v[74:77]
	ds_read_b128 v[126:129], v160 offset:57344
	v_mfma_f32_16x16x32_f16 v[18:21], v[138:141], v[94:97], v[18:21]
	ds_read_b128 v[130:133], v160 offset:59392
	v_mfma_f32_16x16x32_f16 v[26:29], v[142:145], v[94:97], v[26:29]
	v_mfma_f32_16x16x32_f16 v[70:73], v[134:137], v[98:101], v[70:73]
	v_mfma_f32_16x16x32_f16 v[46:49], v[138:141], v[98:101], v[46:49]
	v_mfma_f32_16x16x32_f16 v[240:243], v[142:145], v[98:101], v[240:243]
	v_mfma_f32_16x16x32_f16 v[66:69], v[134:137], v[102:105], v[66:69]
	v_mfma_f32_16x16x32_f16 v[42:45], v[138:141], v[102:105], v[42:45]
	v_mfma_f32_16x16x32_f16 v[236:239], v[142:145], v[102:105], v[236:239]
	v_mfma_f32_16x16x32_f16 v[62:65], v[134:137], v[106:109], v[62:65]
	v_mfma_f32_16x16x32_f16 v[38:41], v[138:141], v[106:109], v[38:41]
	v_mfma_f32_16x16x32_f16 v[34:37], v[142:145], v[106:109], v[34:37]
	s_waitcnt vmcnt(6) lgkmcnt(0)
	s_barrier
	s_add_u32 m0, s11, 0xbf80
	ds_read_b128 v[134:137], v163
	global_load_lds_dwordx4 v[218:219], off offset:128
	v_mfma_f32_16x16x32_f16 v[82:85], v[146:149], v[110:113], v[82:85]
	ds_read_b128 v[138:141], v163 offset:2048
	v_mfma_f32_16x16x32_f16 v[58:61], v[150:153], v[110:113], v[58:61]
	ds_read_b128 v[142:145], v163 offset:4096
	v_mfma_f32_16x16x32_f16 v[14:17], v[154:157], v[110:113], v[14:17]
	s_add_u32 m0, s11, 0xdf80
	ds_read_b128 v[86:89], v159
	global_load_lds_dwordx4 v[222:223], off offset:128
	v_mfma_f32_16x16x32_f16 v[78:81], v[146:149], v[114:117], v[78:81]
	ds_read_b128 v[90:93], v159 offset:2048
	v_mfma_f32_16x16x32_f16 v[22:25], v[150:153], v[114:117], v[22:25]
	ds_read_b128 v[94:97], v159 offset:4096
	v_mfma_f32_16x16x32_f16 v[30:33], v[154:157], v[114:117], v[30:33]
	s_add_u32 m0, s11, 0xff80
	ds_read_b128 v[98:101], v159 offset:6144
	global_load_lds_dwordx4 v[226:227], off offset:128
	v_mfma_f32_16x16x32_f16 v[74:77], v[146:149], v[118:121], v[74:77]
	ds_read_b128 v[102:105], v159 offset:8192
	v_mfma_f32_16x16x32_f16 v[18:21], v[150:153], v[118:121], v[18:21]
	ds_read_b128 v[106:109], v159 offset:10240
	v_mfma_f32_16x16x32_f16 v[26:29], v[154:157], v[118:121], v[26:29]
	v_mfma_f32_16x16x32_f16 v[70:73], v[146:149], v[122:125], v[70:73]
	v_mfma_f32_16x16x32_f16 v[46:49], v[150:153], v[122:125], v[46:49]
	v_mfma_f32_16x16x32_f16 v[240:243], v[154:157], v[122:125], v[240:243]
	v_mfma_f32_16x16x32_f16 v[66:69], v[146:149], v[126:129], v[66:69]
	v_mfma_f32_16x16x32_f16 v[42:45], v[150:153], v[126:129], v[42:45]
	v_mfma_f32_16x16x32_f16 v[236:239], v[154:157], v[126:129], v[236:239]
	v_mfma_f32_16x16x32_f16 v[62:65], v[146:149], v[130:133], v[62:65]
	v_mfma_f32_16x16x32_f16 v[38:41], v[150:153], v[130:133], v[38:41]
	v_mfma_f32_16x16x32_f16 v[34:37], v[154:157], v[130:133], v[34:37]
	s_waitcnt lgkmcnt(0)
	s_add_u32 m0, s11, 0x11f80
	ds_read_b128 v[146:149], v165
	global_load_lds_dwordx4 v[220:221], off offset:128
	v_mfma_f32_16x16x32_f16 v[82:85], v[134:137], v[86:89], v[82:85]
	ds_read_b128 v[150:153], v165 offset:2048
	v_mfma_f32_16x16x32_f16 v[58:61], v[138:141], v[86:89], v[58:61]
	ds_read_b128 v[154:157], v165 offset:4096
	v_mfma_f32_16x16x32_f16 v[14:17], v[142:145], v[86:89], v[14:17]
	s_add_u32 m0, s11, 0x13f80
	ds_read_b128 v[110:113], v161
	global_load_lds_dwordx4 v[224:225], off offset:128
	v_mfma_f32_16x16x32_f16 v[78:81], v[134:137], v[90:93], v[78:81]
	ds_read_b128 v[114:117], v161 offset:2048
	v_mfma_f32_16x16x32_f16 v[22:25], v[138:141], v[90:93], v[22:25]
	ds_read_b128 v[118:121], v161 offset:4096
	v_mfma_f32_16x16x32_f16 v[30:33], v[142:145], v[90:93], v[30:33]
	s_add_u32 m0, s11, 0x15f80
	ds_read_b128 v[122:125], v161 offset:6144
	global_load_lds_dwordx4 v[228:229], off offset:128
	v_mfma_f32_16x16x32_f16 v[74:77], v[134:137], v[94:97], v[74:77]
	ds_read_b128 v[126:129], v161 offset:8192
	v_mfma_f32_16x16x32_f16 v[18:21], v[138:141], v[94:97], v[18:21]
	ds_read_b128 v[130:133], v161 offset:10240
	v_mfma_f32_16x16x32_f16 v[26:29], v[142:145], v[94:97], v[26:29]
	v_mfma_f32_16x16x32_f16 v[70:73], v[134:137], v[98:101], v[70:73]
	v_mfma_f32_16x16x32_f16 v[46:49], v[138:141], v[98:101], v[46:49]
	v_mfma_f32_16x16x32_f16 v[240:243], v[142:145], v[98:101], v[240:243]
	v_mfma_f32_16x16x32_f16 v[66:69], v[134:137], v[102:105], v[66:69]
	v_mfma_f32_16x16x32_f16 v[42:45], v[138:141], v[102:105], v[42:45]
	v_mfma_f32_16x16x32_f16 v[236:239], v[142:145], v[102:105], v[236:239]
	v_mfma_f32_16x16x32_f16 v[62:65], v[134:137], v[106:109], v[62:65]
	v_mfma_f32_16x16x32_f16 v[38:41], v[138:141], v[106:109], v[38:41]
	v_mfma_f32_16x16x32_f16 v[34:37], v[142:145], v[106:109], v[34:37]
	s_waitcnt vmcnt(6) lgkmcnt(0)
	s_barrier
	s_add_u32 m0, s11, 0x17f00
	ds_read_b128 v[134:137], v162
	global_load_lds_dwordx4 v[218:219], off offset:256
	v_mfma_f32_16x16x32_f16 v[82:85], v[146:149], v[110:113], v[82:85]
	ds_read_b128 v[138:141], v162 offset:2048
	v_mfma_f32_16x16x32_f16 v[58:61], v[150:153], v[110:113], v[58:61]
	ds_read_b128 v[142:145], v162 offset:4096
	v_mfma_f32_16x16x32_f16 v[14:17], v[154:157], v[110:113], v[14:17]
	s_add_u32 m0, s11, 0x19f00
	ds_read_b128 v[86:89], v158
	global_load_lds_dwordx4 v[222:223], off offset:256
	v_mfma_f32_16x16x32_f16 v[78:81], v[146:149], v[114:117], v[78:81]
	ds_read_b128 v[90:93], v158 offset:2048
	v_mfma_f32_16x16x32_f16 v[22:25], v[150:153], v[114:117], v[22:25]
	ds_read_b128 v[94:97], v158 offset:4096
	v_mfma_f32_16x16x32_f16 v[30:33], v[154:157], v[114:117], v[30:33]
	s_add_u32 m0, s11, 0x1bf00
	ds_read_b128 v[98:101], v158 offset:6144
	global_load_lds_dwordx4 v[226:227], off offset:256
	v_mfma_f32_16x16x32_f16 v[74:77], v[146:149], v[118:121], v[74:77]
	ds_read_b128 v[102:105], v158 offset:8192
	v_mfma_f32_16x16x32_f16 v[18:21], v[150:153], v[118:121], v[18:21]
	ds_read_b128 v[106:109], v158 offset:10240
	v_mfma_f32_16x16x32_f16 v[26:29], v[154:157], v[118:121], v[26:29]
	v_mfma_f32_16x16x32_f16 v[70:73], v[146:149], v[122:125], v[70:73]
	v_mfma_f32_16x16x32_f16 v[46:49], v[150:153], v[122:125], v[46:49]
	v_mfma_f32_16x16x32_f16 v[240:243], v[154:157], v[122:125], v[240:243]
	v_mfma_f32_16x16x32_f16 v[66:69], v[146:149], v[126:129], v[66:69]
	v_mfma_f32_16x16x32_f16 v[42:45], v[150:153], v[126:129], v[42:45]
	v_mfma_f32_16x16x32_f16 v[236:239], v[154:157], v[126:129], v[236:239]
	v_mfma_f32_16x16x32_f16 v[62:65], v[146:149], v[130:133], v[62:65]
	v_mfma_f32_16x16x32_f16 v[38:41], v[150:153], v[130:133], v[38:41]
	v_mfma_f32_16x16x32_f16 v[34:37], v[154:157], v[130:133], v[34:37]
	v_lshl_add_u64 v[218:219], v[218:219], 0, s[20:21]
	v_lshl_add_u64 v[222:223], v[222:223], 0, s[20:21]
	v_lshl_add_u64 v[226:227], v[226:227], 0, s[20:21]
	v_lshl_add_u64 v[220:221], v[220:221], 0, s[20:21]
	v_lshl_add_u64 v[224:225], v[224:225], 0, s[20:21]
	v_lshl_add_u64 v[228:229], v[228:229], 0, s[20:21]
	s_sub_u32 s22, s22, 1
	s_cmp_lg_u32 s22, 0
	s_cbranch_scc1 .Lgemm_T_loop
	s_waitcnt lgkmcnt(0)
	s_add_u32 m0, s11, 0x1e080
	ds_read_b128 v[146:149], v164
	global_load_lds_dwordx4 v[220:221], off offset:-128
	v_mfma_f32_16x16x32_f16 v[82:85], v[134:137], v[86:89], v[82:85]
	ds_read_b128 v[150:153], v164 offset:2048
	v_mfma_f32_16x16x32_f16 v[58:61], v[138:141], v[86:89], v[58:61]
	ds_read_b128 v[154:157], v164 offset:4096
	v_mfma_f32_16x16x32_f16 v[14:17], v[142:145], v[86:89], v[14:17]
	s_add_u32 m0, s11, 0x20080
	ds_read_b128 v[110:113], v160
	global_load_lds_dwordx4 v[224:225], off offset:-128
	v_mfma_f32_16x16x32_f16 v[78:81], v[134:137], v[90:93], v[78:81]
	ds_read_b128 v[114:117], v160 offset:2048
	v_mfma_f32_16x16x32_f16 v[22:25], v[138:141], v[90:93], v[22:25]
	ds_read_b128 v[118:121], v160 offset:4096
	v_mfma_f32_16x16x32_f16 v[30:33], v[142:145], v[90:93], v[30:33]
	s_add_u32 m0, s11, 0x22080
	ds_read_b128 v[122:125], v160 offset:6144
	global_load_lds_dwordx4 v[228:229], off offset:-128
	v_mfma_f32_16x16x32_f16 v[74:77], v[134:137], v[94:97], v[74:77]
	ds_read_b128 v[126:129], v160 offset:8192
	v_mfma_f32_16x16x32_f16 v[18:21], v[138:141], v[94:97], v[18:21]
	ds_read_b128 v[130:133], v160 offset:10240
	v_mfma_f32_16x16x32_f16 v[26:29], v[142:145], v[94:97], v[26:29]
	v_mfma_f32_16x16x32_f16 v[70:73], v[134:137], v[98:101], v[70:73]
	v_mfma_f32_16x16x32_f16 v[46:49], v[138:141], v[98:101], v[46:49]
	v_mfma_f32_16x16x32_f16 v[240:243], v[142:145], v[98:101], v[240:243]
	v_mfma_f32_16x16x32_f16 v[66:69], v[134:137], v[102:105], v[66:69]
	v_mfma_f32_16x16x32_f16 v[42:45], v[138:141], v[102:105], v[42:45]
	v_mfma_f32_16x16x32_f16 v[236:239], v[142:145], v[102:105], v[236:239]
	v_mfma_f32_16x16x32_f16 v[62:65], v[134:137], v[106:109], v[62:65]
	v_mfma_f32_16x16x32_f16 v[38:41], v[138:141], v[106:109], v[38:41]
	v_mfma_f32_16x16x32_f16 v[34:37], v[142:145], v[106:109], v[34:37]
	s_waitcnt vmcnt(6) lgkmcnt(0)
	s_barrier
	s_add_u32 m0, s11, 0x0
	ds_read_b128 v[134:137], v162 offset:49152
	global_load_lds_dwordx4 v[218:219], off
	v_mfma_f32_16x16x32_f16 v[82:85], v[146:149], v[110:113], v[82:85]
	ds_read_b128 v[138:141], v162 offset:51200
	v_mfma_f32_16x16x32_f16 v[58:61], v[150:153], v[110:113], v[58:61]
	ds_read_b128 v[142:145], v162 offset:53248
	v_mfma_f32_16x16x32_f16 v[14:17], v[154:157], v[110:113], v[14:17]
	s_add_u32 m0, s11, 0x2000
	ds_read_b128 v[86:89], v158 offset:49152
	global_load_lds_dwordx4 v[222:223], off
	v_mfma_f32_16x16x32_f16 v[78:81], v[146:149], v[114:117], v[78:81]
	ds_read_b128 v[90:93], v158 offset:51200
	v_mfma_f32_16x16x32_f16 v[22:25], v[150:153], v[114:117], v[22:25]
	ds_read_b128 v[94:97], v158 offset:53248
	v_mfma_f32_16x16x32_f16 v[30:33], v[154:157], v[114:117], v[30:33]
	s_add_u32 m0, s11, 0x4000
	ds_read_b128 v[98:101], v158 offset:55296
	global_load_lds_dwordx4 v[226:227], off
	v_mfma_f32_16x16x32_f16 v[74:77], v[146:149], v[118:121], v[74:77]
	ds_read_b128 v[102:105], v158 offset:57344
	v_mfma_f32_16x16x32_f16 v[18:21], v[150:153], v[118:121], v[18:21]
	ds_read_b128 v[106:109], v158 offset:59392
	v_mfma_f32_16x16x32_f16 v[26:29], v[154:157], v[118:121], v[26:29]
	v_mfma_f32_16x16x32_f16 v[70:73], v[146:149], v[122:125], v[70:73]
	v_mfma_f32_16x16x32_f16 v[46:49], v[150:153], v[122:125], v[46:49]
	v_mfma_f32_16x16x32_f16 v[240:243], v[154:157], v[122:125], v[240:243]
	v_mfma_f32_16x16x32_f16 v[66:69], v[146:149], v[126:129], v[66:69]
	v_mfma_f32_16x16x32_f16 v[42:45], v[150:153], v[126:129], v[42:45]
	v_mfma_f32_16x16x32_f16 v[236:239], v[154:157], v[126:129], v[236:239]
	v_mfma_f32_16x16x32_f16 v[62:65], v[146:149], v[130:133], v[62:65]
	v_mfma_f32_16x16x32_f16 v[38:41], v[150:153], v[130:133], v[38:41]
	v_mfma_f32_16x16x32_f16 v[34:37], v[154:157], v[130:133], v[34:37]
	s_waitcnt lgkmcnt(0)
	s_add_u32 m0, s11, 0x6000
	ds_read_b128 v[146:149], v164 offset:49152
	global_load_lds_dwordx4 v[220:221], off
	v_mfma_f32_16x16x32_f16 v[82:85], v[134:137], v[86:89], v[82:85]
	ds_read_b128 v[150:153], v164 offset:51200
	v_mfma_f32_16x16x32_f16 v[58:61], v[138:141], v[86:89], v[58:61]
	ds_read_b128 v[154:157], v164 offset:53248
	v_mfma_f32_16x16x32_f16 v[14:17], v[142:145], v[86:89], v[14:17]
	s_add_u32 m0, s11, 0x8000
	ds_read_b128 v[110:113], v160 offset:49152
	global_load_lds_dwordx4 v[224:225], off
	v_mfma_f32_16x16x32_f16 v[78:81], v[134:137], v[90:93], v[78:81]
	ds_read_b128 v[114:117], v160 offset:51200
	v_mfma_f32_16x16x32_f16 v[22:25], v[138:141], v[90:93], v[22:25]
	ds_read_b128 v[118:121], v160 offset:53248
	v_mfma_f32_16x16x32_f16 v[30:33], v[142:145], v[90:93], v[30:33]
	s_add_u32 m0, s11, 0xa000
	ds_read_b128 v[122:125], v160 offset:55296
	global_load_lds_dwordx4 v[228:229], off
	v_mfma_f32_16x16x32_f16 v[74:77], v[134:137], v[94:97], v[74:77]
	ds_read_b128 v[126:129], v160 offset:57344
	v_mfma_f32_16x16x32_f16 v[18:21], v[138:141], v[94:97], v[18:21]
	ds_read_b128 v[130:133], v160 offset:59392
	v_mfma_f32_16x16x32_f16 v[26:29], v[142:145], v[94:97], v[26:29]
	v_mfma_f32_16x16x32_f16 v[70:73], v[134:137], v[98:101], v[70:73]
	v_mfma_f32_16x16x32_f16 v[46:49], v[138:141], v[98:101], v[46:49]
	v_mfma_f32_16x16x32_f16 v[240:243], v[142:145], v[98:101], v[240:243]
	v_mfma_f32_16x16x32_f16 v[66:69], v[134:137], v[102:105], v[66:69]
	v_mfma_f32_16x16x32_f16 v[42:45], v[138:141], v[102:105], v[42:45]
	v_mfma_f32_16x16x32_f16 v[236:239], v[142:145], v[102:105], v[236:239]
	v_mfma_f32_16x16x32_f16 v[62:65], v[134:137], v[106:109], v[62:65]
	v_mfma_f32_16x16x32_f16 v[38:41], v[138:141], v[106:109], v[38:41]
	v_mfma_f32_16x16x32_f16 v[34:37], v[142:145], v[106:109], v[34:37]
	s_waitcnt vmcnt(6) lgkmcnt(0)
	s_barrier
	s_lshl_b32 s26, s17, 2
	s_add_u32 s26, s24, s26
	s_addc_u32 s27, s25, 0
	v_lshlrev_b32_e32 v50, 4, v231
	global_load_dwordx4 v[10:13], v50, s[26:27]
	global_load_dwordx4 v[6:9], v50, s[26:27] offset:64
	global_load_dwordx4 v[2:5], v50, s[26:27] offset:128
	ds_read_b128 v[134:137], v163
	v_mfma_f32_16x16x32_f16 v[82:85], v[146:149], v[110:113], v[82:85]
	ds_read_b128 v[138:141], v163 offset:2048
	v_mfma_f32_16x16x32_f16 v[58:61], v[150:153], v[110:113], v[58:61]
	ds_read_b128 v[142:145], v163 offset:4096
	v_mfma_f32_16x16x32_f16 v[14:17], v[154:157], v[110:113], v[14:17]
	ds_read_b128 v[86:89], v159
	v_mfma_f32_16x16x32_f16 v[78:81], v[146:149], v[114:117], v[78:81]
	ds_read_b128 v[90:93], v159 offset:2048
	v_mfma_f32_16x16x32_f16 v[22:25], v[150:153], v[114:117], v[22:25]
	ds_read_b128 v[94:97], v159 offset:4096
	v_mfma_f32_16x16x32_f16 v[30:33], v[154:157], v[114:117], v[30:33]
	ds_read_b128 v[98:101], v159 offset:6144
	v_mfma_f32_16x16x32_f16 v[74:77], v[146:149], v[118:121], v[74:77]
	ds_read_b128 v[102:105], v159 offset:8192
	v_mfma_f32_16x16x32_f16 v[18:21], v[150:153], v[118:121], v[18:21]
	ds_read_b128 v[106:109], v159 offset:10240
	v_mfma_f32_16x16x32_f16 v[26:29], v[154:157], v[118:121], v[26:29]
	v_mfma_f32_16x16x32_f16 v[70:73], v[146:149], v[122:125], v[70:73]
	v_mfma_f32_16x16x32_f16 v[46:49], v[150:153], v[122:125], v[46:49]
	v_mfma_f32_16x16x32_f16 v[240:243], v[154:157], v[122:125], v[240:243]
	v_mfma_f32_16x16x32_f16 v[66:69], v[146:149], v[126:129], v[66:69]
	v_mfma_f32_16x16x32_f16 v[42:45], v[150:153], v[126:129], v[42:45]
	v_mfma_f32_16x16x32_f16 v[236:239], v[154:157], v[126:129], v[236:239]
	v_mfma_f32_16x16x32_f16 v[62:65], v[146:149], v[130:133], v[62:65]
	v_mfma_f32_16x16x32_f16 v[38:41], v[150:153], v[130:133], v[38:41]
	v_mfma_f32_16x16x32_f16 v[34:37], v[154:157], v[130:133], v[34:37]
	s_waitcnt lgkmcnt(0)
	ds_read_b128 v[146:149], v165
	v_mfma_f32_16x16x32_f16 v[82:85], v[134:137], v[86:89], v[82:85]
	ds_read_b128 v[150:153], v165 offset:2048
	v_mfma_f32_16x16x32_f16 v[58:61], v[138:141], v[86:89], v[58:61]
	ds_read_b128 v[154:157], v165 offset:4096
	v_mfma_f32_16x16x32_f16 v[14:17], v[142:145], v[86:89], v[14:17]
	ds_read_b128 v[110:113], v161
	v_mfma_f32_16x16x32_f16 v[78:81], v[134:137], v[90:93], v[78:81]
	ds_read_b128 v[114:117], v161 offset:2048
	v_mfma_f32_16x16x32_f16 v[22:25], v[138:141], v[90:93], v[22:25]
	ds_read_b128 v[118:121], v161 offset:4096
	v_mfma_f32_16x16x32_f16 v[30:33], v[142:145], v[90:93], v[30:33]
	ds_read_b128 v[122:125], v161 offset:6144
	v_mfma_f32_16x16x32_f16 v[74:77], v[134:137], v[94:97], v[74:77]
	ds_read_b128 v[126:129], v161 offset:8192
	v_mfma_f32_16x16x32_f16 v[18:21], v[138:141], v[94:97], v[18:21]
	ds_read_b128 v[130:133], v161 offset:10240
	v_mfma_f32_16x16x32_f16 v[26:29], v[142:145], v[94:97], v[26:29]
	v_mfma_f32_16x16x32_f16 v[70:73], v[134:137], v[98:101], v[70:73]
	v_mfma_f32_16x16x32_f16 v[46:49], v[138:141], v[98:101], v[46:49]
	v_mfma_f32_16x16x32_f16 v[240:243], v[142:145], v[98:101], v[240:243]
	v_mfma_f32_16x16x32_f16 v[66:69], v[134:137], v[102:105], v[66:69]
	v_mfma_f32_16x16x32_f16 v[42:45], v[138:141], v[102:105], v[42:45]
	v_mfma_f32_16x16x32_f16 v[236:239], v[142:145], v[102:105], v[236:239]
	v_mfma_f32_16x16x32_f16 v[62:65], v[134:137], v[106:109], v[62:65]
	v_mfma_f32_16x16x32_f16 v[38:41], v[138:141], v[106:109], v[38:41]
	v_mfma_f32_16x16x32_f16 v[34:37], v[142:145], v[106:109], v[34:37]
	s_waitcnt vmcnt(3) lgkmcnt(0)
	s_barrier
	ds_read_b128 v[134:137], v162
	v_mfma_f32_16x16x32_f16 v[82:85], v[146:149], v[110:113], v[82:85]
	ds_read_b128 v[138:141], v162 offset:2048
	v_mfma_f32_16x16x32_f16 v[58:61], v[150:153], v[110:113], v[58:61]
	ds_read_b128 v[142:145], v162 offset:4096
	v_mfma_f32_16x16x32_f16 v[14:17], v[154:157], v[110:113], v[14:17]
	ds_read_b128 v[86:89], v158
	v_mfma_f32_16x16x32_f16 v[78:81], v[146:149], v[114:117], v[78:81]
	ds_read_b128 v[90:93], v158 offset:2048
	v_mfma_f32_16x16x32_f16 v[22:25], v[150:153], v[114:117], v[22:25]
	ds_read_b128 v[94:97], v158 offset:4096
	v_mfma_f32_16x16x32_f16 v[30:33], v[154:157], v[114:117], v[30:33]
	ds_read_b128 v[98:101], v158 offset:6144
	v_mfma_f32_16x16x32_f16 v[74:77], v[146:149], v[118:121], v[74:77]
	ds_read_b128 v[102:105], v158 offset:8192
	v_mfma_f32_16x16x32_f16 v[18:21], v[150:153], v[118:121], v[18:21]
	ds_read_b128 v[106:109], v158 offset:10240
	v_mfma_f32_16x16x32_f16 v[26:29], v[154:157], v[118:121], v[26:29]
	v_mfma_f32_16x16x32_f16 v[70:73], v[146:149], v[122:125], v[70:73]
	v_mfma_f32_16x16x32_f16 v[46:49], v[150:153], v[122:125], v[46:49]
	v_mfma_f32_16x16x32_f16 v[240:243], v[154:157], v[122:125], v[240:243]
	v_mfma_f32_16x16x32_f16 v[66:69], v[146:149], v[126:129], v[66:69]
	v_mfma_f32_16x16x32_f16 v[42:45], v[150:153], v[126:129], v[42:45]
	v_mfma_f32_16x16x32_f16 v[236:239], v[154:157], v[126:129], v[236:239]
	v_mfma_f32_16x16x32_f16 v[62:65], v[146:149], v[130:133], v[62:65]
	v_mfma_f32_16x16x32_f16 v[38:41], v[150:153], v[130:133], v[38:41]
	v_mfma_f32_16x16x32_f16 v[34:37], v[154:157], v[130:133], v[34:37]
	s_waitcnt lgkmcnt(0)
	ds_read_b128 v[146:149], v164
	v_mfma_f32_16x16x32_f16 v[82:85], v[134:137], v[86:89], v[82:85]
	ds_read_b128 v[150:153], v164 offset:2048
	v_mfma_f32_16x16x32_f16 v[58:61], v[138:141], v[86:89], v[58:61]
	ds_read_b128 v[154:157], v164 offset:4096
	v_mfma_f32_16x16x32_f16 v[14:17], v[142:145], v[86:89], v[14:17]
	ds_read_b128 v[110:113], v160
	v_mfma_f32_16x16x32_f16 v[78:81], v[134:137], v[90:93], v[78:81]
	ds_read_b128 v[114:117], v160 offset:2048
	v_mfma_f32_16x16x32_f16 v[22:25], v[138:141], v[90:93], v[22:25]
	ds_read_b128 v[118:121], v160 offset:4096
	v_mfma_f32_16x16x32_f16 v[30:33], v[142:145], v[90:93], v[30:33]
	ds_read_b128 v[122:125], v160 offset:6144
	v_mfma_f32_16x16x32_f16 v[74:77], v[134:137], v[94:97], v[74:77]
	ds_read_b128 v[126:129], v160 offset:8192
	v_mfma_f32_16x16x32_f16 v[18:21], v[138:141], v[94:97], v[18:21]
	ds_read_b128 v[130:133], v160 offset:10240
	v_mfma_f32_16x16x32_f16 v[26:29], v[142:145], v[94:97], v[26:29]
	v_mfma_f32_16x16x32_f16 v[70:73], v[134:137], v[98:101], v[70:73]
	v_mfma_f32_16x16x32_f16 v[46:49], v[138:141], v[98:101], v[46:49]
	v_mfma_f32_16x16x32_f16 v[240:243], v[142:145], v[98:101], v[240:243]
	v_mfma_f32_16x16x32_f16 v[66:69], v[134:137], v[102:105], v[66:69]
	v_mfma_f32_16x16x32_f16 v[42:45], v[138:141], v[102:105], v[42:45]
	v_mfma_f32_16x16x32_f16 v[236:239], v[142:145], v[102:105], v[236:239]
	v_mfma_f32_16x16x32_f16 v[62:65], v[134:137], v[106:109], v[62:65]
	v_mfma_f32_16x16x32_f16 v[38:41], v[138:141], v[106:109], v[38:41]
	v_mfma_f32_16x16x32_f16 v[34:37], v[142:145], v[106:109], v[34:37]
	s_waitcnt lgkmcnt(0)
	v_mfma_f32_16x16x32_f16 v[82:85], v[146:149], v[110:113], v[82:85]
	v_mfma_f32_16x16x32_f16 v[58:61], v[150:153], v[110:113], v[58:61]
	v_mfma_f32_16x16x32_f16 v[14:17], v[154:157], v[110:113], v[14:17]
	v_mfma_f32_16x16x32_f16 v[78:81], v[146:149], v[114:117], v[78:81]
	v_mfma_f32_16x16x32_f16 v[22:25], v[150:153], v[114:117], v[22:25]
	v_mfma_f32_16x16x32_f16 v[30:33], v[154:157], v[114:117], v[30:33]
	v_mfma_f32_16x16x32_f16 v[74:77], v[146:149], v[118:121], v[74:77]
	v_mfma_f32_16x16x32_f16 v[18:21], v[150:153], v[118:121], v[18:21]
	v_mfma_f32_16x16x32_f16 v[26:29], v[154:157], v[118:121], v[26:29]
	v_mfma_f32_16x16x32_f16 v[70:73], v[146:149], v[122:125], v[70:73]
	v_mfma_f32_16x16x32_f16 v[46:49], v[150:153], v[122:125], v[46:49]
	v_mfma_f32_16x16x32_f16 v[240:243], v[154:157], v[122:125], v[240:243]
	v_mfma_f32_16x16x32_f16 v[66:69], v[146:149], v[126:129], v[66:69]
	v_mfma_f32_16x16x32_f16 v[42:45], v[150:153], v[126:129], v[42:45]
	v_mfma_f32_16x16x32_f16 v[236:239], v[154:157], v[126:129], v[236:239]
	v_mfma_f32_16x16x32_f16 v[62:65], v[146:149], v[130:133], v[62:65]
	v_mfma_f32_16x16x32_f16 v[38:41], v[150:153], v[130:133], v[38:41]
	v_mfma_f32_16x16x32_f16 v[34:37], v[154:157], v[130:133], v[34:37]
	s_branch .LBB1_76
.Lgemm_N_loop:
	s_waitcnt lgkmcnt(0)
	s_add_u32 m0, s11, 0x1e080
	ds_read_b128 v[146:149], v164
	global_load_lds_dwordx4 v[220:221], off offset:-128
	v_mfma_f32_16x16x32_f16 v[82:85], v[86:89], v[134:137], v[82:85]
	ds_read_b128 v[150:153], v164 offset:2048
	v_mfma_f32_16x16x32_f16 v[58:61], v[86:89], v[138:141], v[58:61]
	ds_read_b128 v[154:157], v164 offset:4096
	v_mfma_f32_16x16x32_f16 v[14:17], v[86:89], v[142:145], v[14:17]
	s_add_u32 m0, s11, 0x20080
	ds_read_b128 v[110:113], v160
	global_load_lds_dwordx4 v[224:225], off offset:-128
	v_mfma_f32_16x16x32_f16 v[78:81], v[90:93], v[134:137], v[78:81]
	ds_read_b128 v[114:117], v160 offset:2048
	v_mfma_f32_16x16x32_f16 v[22:25], v[90:93], v[138:141], v[22:25]
	ds_read_b128 v[118:121], v160 offset:4096
	v_mfma_f32_16x16x32_f16 v[30:33], v[90:93], v[142:145], v[30:33]
	s_add_u32 m0, s11, 0x22080
	ds_read_b128 v[122:125], v160 offset:6144
	global_load_lds_dwordx4 v[228:229], off offset:-128
	v_mfma_f32_16x16x32_f16 v[74:77], v[94:97], v[134:137], v[74:77]
	ds_read_b128 v[126:129], v160 offset:8192
	v_mfma_f32_16x16x32_f16 v[18:21], v[94:97], v[138:141], v[18:21]
	ds_read_b128 v[130:133], v160 offset:10240
	v_mfma_f32_16x16x32_f16 v[26:29], v[94:97], v[142:145], v[26:29]
	v_mfma_f32_16x16x32_f16 v[70:73], v[98:101], v[134:137], v[70:73]
	v_mfma_f32_16x16x32_f16 v[46:49], v[98:101], v[138:141], v[46:49]
	v_mfma_f32_16x16x32_f16 v[240:243], v[98:101], v[142:145], v[240:243]
	v_mfma_f32_16x16x32_f16 v[66:69], v[102:105], v[134:137], v[66:69]
	v_mfma_f32_16x16x32_f16 v[42:45], v[102:105], v[138:141], v[42:45]
	v_mfma_f32_16x16x32_f16 v[236:239], v[102:105], v[142:145], v[236:239]
	v_mfma_f32_16x16x32_f16 v[62:65], v[106:109], v[134:137], v[62:65]
	v_mfma_f32_16x16x32_f16 v[38:41], v[106:109], v[138:141], v[38:41]
	v_mfma_f32_16x16x32_f16 v[34:37], v[106:109], v[142:145], v[34:37]
	s_waitcnt vmcnt(6) lgkmcnt(0)
	s_barrier
	s_add_u32 m0, s11, 0x0
	ds_read_b128 v[134:137], v162 offset:49152
	global_load_lds_dwordx4 v[218:219], off
	v_mfma_f32_16x16x32_f16 v[82:85], v[110:113], v[146:149], v[82:85]
	ds_read_b128 v[138:141], v162 offset:51200
	v_mfma_f32_16x16x32_f16 v[58:61], v[110:113], v[150:153], v[58:61]
	ds_read_b128 v[142:145], v162 offset:53248
	v_mfma_f32_16x16x32_f16 v[14:17], v[110:113], v[154:157], v[14:17]
	s_add_u32 m0, s11, 0x2000
	ds_read_b128 v[86:89], v158 offset:49152
	global_load_lds_dwordx4 v[222:223], off
	v_mfma_f32_16x16x32_f16 v[78:81], v[114:117], v[146:149], v[78:81]
	ds_read_b128 v[90:93], v158 offset:51200
	v_mfma_f32_16x16x32_f16 v[22:25], v[114:117], v[150:153], v[22:25]
	ds_read_b128 v[94:97], v158 offset:53248
	v_mfma_f32_16x16x32_f16 v[30:33], v[114:117], v[154:157], v[30:33]
	s_add_u32 m0, s11, 0x4000
	ds_read_b128 v[98:101], v158 offset:55296
	global_load_lds_dwordx4 v[226:227], off
	v_mfma_f32_16x16x32_f16 v[74:77], v[118:121], v[146:149], v[74:77]
	ds_read_b128 v[102:105], v158 offset:57344
	v_mfma_f32_16x16x32_f16 v[18:21], v[118:121], v[150:153], v[18:21]
	ds_read_b128 v[106:109], v158 offset:59392
	v_mfma_f32_16x16x32_f16 v[26:29], v[118:121], v[154:157], v[26:29]
	v_mfma_f32_16x16x32_f16 v[70:73], v[122:125], v[146:149], v[70:73]
	v_mfma_f32_16x16x32_f16 v[46:49], v[122:125], v[150:153], v[46:49]
	v_mfma_f32_16x16x32_f16 v[240:243], v[122:125], v[154:157], v[240:243]
	v_mfma_f32_16x16x32_f16 v[66:69], v[126:129], v[146:149], v[66:69]
	v_mfma_f32_16x16x32_f16 v[42:45], v[126:129], v[150:153], v[42:45]
	v_mfma_f32_16x16x32_f16 v[236:239], v[126:129], v[154:157], v[236:239]
	v_mfma_f32_16x16x32_f16 v[62:65], v[130:133], v[146:149], v[62:65]
	v_mfma_f32_16x16x32_f16 v[38:41], v[130:133], v[150:153], v[38:41]
	v_mfma_f32_16x16x32_f16 v[34:37], v[130:133], v[154:157], v[34:37]
	s_waitcnt lgkmcnt(0)
	s_add_u32 m0, s11, 0x6000
	ds_read_b128 v[146:149], v164 offset:49152
	global_load_lds_dwordx4 v[220:221], off
	v_mfma_f32_16x16x32_f16 v[82:85], v[86:89], v[134:137], v[82:85]
	ds_read_b128 v[150:153], v164 offset:51200
	v_mfma_f32_16x16x32_f16 v[58:61], v[86:89], v[138:141], v[58:61]
	ds_read_b128 v[154:157], v164 offset:53248
	v_mfma_f32_16x16x32_f16 v[14:17], v[86:89], v[142:145], v[14:17]
	s_add_u32 m0, s11, 0x8000
	ds_read_b128 v[110:113], v160 offset:49152
	global_load_lds_dwordx4 v[224:225], off
	v_mfma_f32_16x16x32_f16 v[78:81], v[90:93], v[134:137], v[78:81]
	ds_read_b128 v[114:117], v160 offset:51200
	v_mfma_f32_16x16x32_f16 v[22:25], v[90:93], v[138:141], v[22:25]
	ds_read_b128 v[118:121], v160 offset:53248
	v_mfma_f32_16x16x32_f16 v[30:33], v[90:93], v[142:145], v[30:33]
	s_add_u32 m0, s11, 0xa000
	ds_read_b128 v[122:125], v160 offset:55296
	global_load_lds_dwordx4 v[228:229], off
	v_mfma_f32_16x16x32_f16 v[74:77], v[94:97], v[134:137], v[74:77]
	ds_read_b128 v[126:129], v160 offset:57344
	v_mfma_f32_16x16x32_f16 v[18:21], v[94:97], v[138:141], v[18:21]
	ds_read_b128 v[130:133], v160 offset:59392
	v_mfma_f32_16x16x32_f16 v[26:29], v[94:97], v[142:145], v[26:29]
	v_mfma_f32_16x16x32_f16 v[70:73], v[98:101], v[134:137], v[70:73]
	v_mfma_f32_16x16x32_f16 v[46:49], v[98:101], v[138:141], v[46:49]
	v_mfma_f32_16x16x32_f16 v[240:243], v[98:101], v[142:145], v[240:243]
	v_mfma_f32_16x16x32_f16 v[66:69], v[102:105], v[134:137], v[66:69]
	v_mfma_f32_16x16x32_f16 v[42:45], v[102:105], v[138:141], v[42:45]
	v_mfma_f32_16x16x32_f16 v[236:239], v[102:105], v[142:145], v[236:239]
	v_mfma_f32_16x16x32_f16 v[62:65], v[106:109], v[134:137], v[62:65]
	v_mfma_f32_16x16x32_f16 v[38:41], v[106:109], v[138:141], v[38:41]
	v_mfma_f32_16x16x32_f16 v[34:37], v[106:109], v[142:145], v[34:37]
	s_waitcnt vmcnt(6) lgkmcnt(0)
	s_barrier
	s_add_u32 m0, s11, 0xbf80
	ds_read_b128 v[134:137], v163
	global_load_lds_dwordx4 v[218:219], off offset:128
	v_mfma_f32_16x16x32_f16 v[82:85], v[110:113], v[146:149], v[82:85]
	ds_read_b128 v[138:141], v163 offset:2048
	v_mfma_f32_16x16x32_f16 v[58:61], v[110:113], v[150:153], v[58:61]
	ds_read_b128 v[142:145], v163 offset:4096
	v_mfma_f32_16x16x32_f16 v[14:17], v[110:113], v[154:157], v[14:17]
	s_add_u32 m0, s11, 0xdf80
	ds_read_b128 v[86:89], v159
	global_load_lds_dwordx4 v[222:223], off offset:128
	v_mfma_f32_16x16x32_f16 v[78:81], v[114:117], v[146:149], v[78:81]
	ds_read_b128 v[90:93], v159 offset:2048
	v_mfma_f32_16x16x32_f16 v[22:25], v[114:117], v[150:153], v[22:25]
	ds_read_b128 v[94:97], v159 offset:4096
	v_mfma_f32_16x16x32_f16 v[30:33], v[114:117], v[154:157], v[30:33]
	s_add_u32 m0, s11, 0xff80
	ds_read_b128 v[98:101], v159 offset:6144
	global_load_lds_dwordx4 v[226:227], off offset:128
	v_mfma_f32_16x16x32_f16 v[74:77], v[118:121], v[146:149], v[74:77]
	ds_read_b128 v[102:105], v159 offset:8192
	v_mfma_f32_16x16x32_f16 v[18:21], v[118:121], v[150:153], v[18:21]
	ds_read_b128 v[106:109], v159 offset:10240
	v_mfma_f32_16x16x32_f16 v[26:29], v[118:121], v[154:157], v[26:29]
	v_mfma_f32_16x16x32_f16 v[70:73], v[122:125], v[146:149], v[70:73]
	v_mfma_f32_16x16x32_f16 v[46:49], v[122:125], v[150:153], v[46:49]
	v_mfma_f32_16x16x32_f16 v[240:243], v[122:125], v[154:157], v[240:243]
	v_mfma_f32_16x16x32_f16 v[66:69], v[126:129], v[146:149], v[66:69]
	v_mfma_f32_16x16x32_f16 v[42:45], v[126:129], v[150:153], v[42:45]
	v_mfma_f32_16x16x32_f16 v[236:239], v[126:129], v[154:157], v[236:239]
	v_mfma_f32_16x16x32_f16 v[62:65], v[130:133], v[146:149], v[62:65]
	v_mfma_f32_16x16x32_f16 v[38:41], v[130:133], v[150:153], v[38:41]
	v_mfma_f32_16x16x32_f16 v[34:37], v[130:133], v[154:157], v[34:37]
	s_waitcnt lgkmcnt(0)
	s_add_u32 m0, s11, 0x11f80
	ds_read_b128 v[146:149], v165
	global_load_lds_dwordx4 v[220:221], off offset:128
	v_mfma_f32_16x16x32_f16 v[82:85], v[86:89], v[134:137], v[82:85]
	ds_read_b128 v[150:153], v165 offset:2048
	v_mfma_f32_16x16x32_f16 v[58:61], v[86:89], v[138:141], v[58:61]
	ds_read_b128 v[154:157], v165 offset:4096
	v_mfma_f32_16x16x32_f16 v[14:17], v[86:89], v[142:145], v[14:17]
	s_add_u32 m0, s11, 0x13f80
	ds_read_b128 v[110:113], v161
	global_load_lds_dwordx4 v[224:225], off offset:128
	v_mfma_f32_16x16x32_f16 v[78:81], v[90:93], v[134:137], v[78:81]
	ds_read_b128 v[114:117], v161 offset:2048
	v_mfma_f32_16x16x32_f16 v[22:25], v[90:93], v[138:141], v[22:25]
	ds_read_b128 v[118:121], v161 offset:4096
	v_mfma_f32_16x16x32_f16 v[30:33], v[90:93], v[142:145], v[30:33]
	s_add_u32 m0, s11, 0x15f80
	ds_read_b128 v[122:125], v161 offset:6144
	global_load_lds_dwordx4 v[228:229], off offset:128
	v_mfma_f32_16x16x32_f16 v[74:77], v[94:97], v[134:137], v[74:77]
	ds_read_b128 v[126:129], v161 offset:8192
	v_mfma_f32_16x16x32_f16 v[18:21], v[94:97], v[138:141], v[18:21]
	ds_read_b128 v[130:133], v161 offset:10240
	v_mfma_f32_16x16x32_f16 v[26:29], v[94:97], v[142:145], v[26:29]
	v_mfma_f32_16x16x32_f16 v[70:73], v[98:101], v[134:137], v[70:73]
	v_mfma_f32_16x16x32_f16 v[46:49], v[98:101], v[138:141], v[46:49]
	v_mfma_f32_16x16x32_f16 v[240:243], v[98:101], v[142:145], v[240:243]
	v_mfma_f32_16x16x32_f16 v[66:69], v[102:105], v[134:137], v[66:69]
	v_mfma_f32_16x16x32_f16 v[42:45], v[102:105], v[138:141], v[42:45]
	v_mfma_f32_16x16x32_f16 v[236:239], v[102:105], v[142:145], v[236:239]
	v_mfma_f32_16x16x32_f16 v[62:65], v[106:109], v[134:137], v[62:65]
	v_mfma_f32_16x16x32_f16 v[38:41], v[106:109], v[138:141], v[38:41]
	v_mfma_f32_16x16x32_f16 v[34:37], v[106:109], v[142:145], v[34:37]
	s_waitcnt vmcnt(6) lgkmcnt(0)
	s_barrier
	s_add_u32 m0, s11, 0x17f00
	ds_read_b128 v[134:137], v162
	global_load_lds_dwordx4 v[218:219], off offset:256
	v_mfma_f32_16x16x32_f16 v[82:85], v[110:113], v[146:149], v[82:85]
	ds_read_b128 v[138:141], v162 offset:2048
	v_mfma_f32_16x16x32_f16 v[58:61], v[110:113], v[150:153], v[58:61]
	ds_read_b128 v[142:145], v162 offset:4096
	v_mfma_f32_16x16x32_f16 v[14:17], v[110:113], v[154:157], v[14:17]
	s_add_u32 m0, s11, 0x19f00
	ds_read_b128 v[86:89], v158
	global_load_lds_dwordx4 v[222:223], off offset:256
	v_mfma_f32_16x16x32_f16 v[78:81], v[114:117], v[146:149], v[78:81]
	ds_read_b128 v[90:93], v158 offset:2048
	v_mfma_f32_16x16x32_f16 v[22:25], v[114:117], v[150:153], v[22:25]
	ds_read_b128 v[94:97], v158 offset:4096
	v_mfma_f32_16x16x32_f16 v[30:33], v[114:117], v[154:157], v[30:33]
	s_add_u32 m0, s11, 0x1bf00
	ds_read_b128 v[98:101], v158 offset:6144
	global_load_lds_dwordx4 v[226:227], off offset:256
	v_mfma_f32_16x16x32_f16 v[74:77], v[118:121], v[146:149], v[74:77]
	ds_read_b128 v[102:105], v158 offset:8192
	v_mfma_f32_16x16x32_f16 v[18:21], v[118:121], v[150:153], v[18:21]
	ds_read_b128 v[106:109], v158 offset:10240
	v_mfma_f32_16x16x32_f16 v[26:29], v[118:121], v[154:157], v[26:29]
	v_mfma_f32_16x16x32_f16 v[70:73], v[122:125], v[146:149], v[70:73]
	v_mfma_f32_16x16x32_f16 v[46:49], v[122:125], v[150:153], v[46:49]
	v_mfma_f32_16x16x32_f16 v[240:243], v[122:125], v[154:157], v[240:243]
	v_mfma_f32_16x16x32_f16 v[66:69], v[126:129], v[146:149], v[66:69]
	v_mfma_f32_16x16x32_f16 v[42:45], v[126:129], v[150:153], v[42:45]
	v_mfma_f32_16x16x32_f16 v[236:239], v[126:129], v[154:157], v[236:239]
	v_mfma_f32_16x16x32_f16 v[62:65], v[130:133], v[146:149], v[62:65]
	v_mfma_f32_16x16x32_f16 v[38:41], v[130:133], v[150:153], v[38:41]
	v_mfma_f32_16x16x32_f16 v[34:37], v[130:133], v[154:157], v[34:37]
	v_lshl_add_u64 v[218:219], v[218:219], 0, s[20:21]
	v_lshl_add_u64 v[222:223], v[222:223], 0, s[20:21]
	v_lshl_add_u64 v[226:227], v[226:227], 0, s[20:21]
	v_lshl_add_u64 v[220:221], v[220:221], 0, s[20:21]
	v_lshl_add_u64 v[224:225], v[224:225], 0, s[20:21]
	v_lshl_add_u64 v[228:229], v[228:229], 0, s[20:21]
	s_sub_u32 s22, s22, 1
	s_cmp_lg_u32 s22, 0
	s_cbranch_scc1 .Lgemm_N_loop
	s_waitcnt lgkmcnt(0)
	s_add_u32 m0, s11, 0x1e080
	ds_read_b128 v[146:149], v164
	global_load_lds_dwordx4 v[220:221], off offset:-128
	v_mfma_f32_16x16x32_f16 v[82:85], v[86:89], v[134:137], v[82:85]
	ds_read_b128 v[150:153], v164 offset:2048
	v_mfma_f32_16x16x32_f16 v[58:61], v[86:89], v[138:141], v[58:61]
	ds_read_b128 v[154:157], v164 offset:4096
	v_mfma_f32_16x16x32_f16 v[14:17], v[86:89], v[142:145], v[14:17]
	s_add_u32 m0, s11, 0x20080
	ds_read_b128 v[110:113], v160
	global_load_lds_dwordx4 v[224:225], off offset:-128
	v_mfma_f32_16x16x32_f16 v[78:81], v[90:93], v[134:137], v[78:81]
	ds_read_b128 v[114:117], v160 offset:2048
	v_mfma_f32_16x16x32_f16 v[22:25], v[90:93], v[138:141], v[22:25]
	ds_read_b128 v[118:121], v160 offset:4096
	v_mfma_f32_16x16x32_f16 v[30:33], v[90:93], v[142:145], v[30:33]
	s_add_u32 m0, s11, 0x22080
	ds_read_b128 v[122:125], v160 offset:6144
	global_load_lds_dwordx4 v[228:229], off offset:-128
	v_mfma_f32_16x16x32_f16 v[74:77], v[94:97], v[134:137], v[74:77]
	ds_read_b128 v[126:129], v160 offset:8192
	v_mfma_f32_16x16x32_f16 v[18:21], v[94:97], v[138:141], v[18:21]
	ds_read_b128 v[130:133], v160 offset:10240
	v_mfma_f32_16x16x32_f16 v[26:29], v[94:97], v[142:145], v[26:29]
	v_mfma_f32_16x16x32_f16 v[70:73], v[98:101], v[134:137], v[70:73]
	v_mfma_f32_16x16x32_f16 v[46:49], v[98:101], v[138:141], v[46:49]
	v_mfma_f32_16x16x32_f16 v[240:243], v[98:101], v[142:145], v[240:243]
	v_mfma_f32_16x16x32_f16 v[66:69], v[102:105], v[134:137], v[66:69]
	v_mfma_f32_16x16x32_f16 v[42:45], v[102:105], v[138:141], v[42:45]
	v_mfma_f32_16x16x32_f16 v[236:239], v[102:105], v[142:145], v[236:239]
	v_mfma_f32_16x16x32_f16 v[62:65], v[106:109], v[134:137], v[62:65]
	v_mfma_f32_16x16x32_f16 v[38:41], v[106:109], v[138:141], v[38:41]
	v_mfma_f32_16x16x32_f16 v[34:37], v[106:109], v[142:145], v[34:37]
	s_waitcnt vmcnt(6) lgkmcnt(0)
	s_barrier
	s_add_u32 m0, s11, 0x0
	ds_read_b128 v[134:137], v162 offset:49152
	global_load_lds_dwordx4 v[218:219], off
	v_mfma_f32_16x16x32_f16 v[82:85], v[110:113], v[146:149], v[82:85]
	ds_read_b128 v[138:141], v162 offset:51200
	v_mfma_f32_16x16x32_f16 v[58:61], v[110:113], v[150:153], v[58:61]
	ds_read_b128 v[142:145], v162 offset:53248
	v_mfma_f32_16x16x32_f16 v[14:17], v[110:113], v[154:157], v[14:17]
	s_add_u32 m0, s11, 0x2000
	ds_read_b128 v[86:89], v158 offset:49152
	global_load_lds_dwordx4 v[222:223], off
	v_mfma_f32_16x16x32_f16 v[78:81], v[114:117], v[146:149], v[78:81]
	ds_read_b128 v[90:93], v158 offset:51200
	v_mfma_f32_16x16x32_f16 v[22:25], v[114:117], v[150:153], v[22:25]
	ds_read_b128 v[94:97], v158 offset:53248
	v_mfma_f32_16x16x32_f16 v[30:33], v[114:117], v[154:157], v[30:33]
	s_add_u32 m0, s11, 0x4000
	ds_read_b128 v[98:101], v158 offset:55296
	global_load_lds_dwordx4 v[226:227], off
	v_mfma_f32_16x16x32_f16 v[74:77], v[118:121], v[146:149], v[74:77]
	ds_read_b128 v[102:105], v158 offset:57344
	v_mfma_f32_16x16x32_f16 v[18:21], v[118:121], v[150:153], v[18:21]
	ds_read_b128 v[106:109], v158 offset:59392
	v_mfma_f32_16x16x32_f16 v[26:29], v[118:121], v[154:157], v[26:29]
	v_mfma_f32_16x16x32_f16 v[70:73], v[122:125], v[146:149], v[70:73]
	v_mfma_f32_16x16x32_f16 v[46:49], v[122:125], v[150:153], v[46:49]
	v_mfma_f32_16x16x32_f16 v[240:243], v[122:125], v[154:157], v[240:243]
	v_mfma_f32_16x16x32_f16 v[66:69], v[126:129], v[146:149], v[66:69]
	v_mfma_f32_16x16x32_f16 v[42:45], v[126:129], v[150:153], v[42:45]
	v_mfma_f32_16x16x32_f16 v[236:239], v[126:129], v[154:157], v[236:239]
	v_mfma_f32_16x16x32_f16 v[62:65], v[130:133], v[146:149], v[62:65]
	v_mfma_f32_16x16x32_f16 v[38:41], v[130:133], v[150:153], v[38:41]
	v_mfma_f32_16x16x32_f16 v[34:37], v[130:133], v[154:157], v[34:37]
	s_waitcnt lgkmcnt(0)
	s_add_u32 m0, s11, 0x6000
	ds_read_b128 v[146:149], v164 offset:49152
	global_load_lds_dwordx4 v[220:221], off
	v_mfma_f32_16x16x32_f16 v[82:85], v[86:89], v[134:137], v[82:85]
	ds_read_b128 v[150:153], v164 offset:51200
	v_mfma_f32_16x16x32_f16 v[58:61], v[86:89], v[138:141], v[58:61]
	ds_read_b128 v[154:157], v164 offset:53248
	v_mfma_f32_16x16x32_f16 v[14:17], v[86:89], v[142:145], v[14:17]
	s_add_u32 m0, s11, 0x8000
	ds_read_b128 v[110:113], v160 offset:49152
	global_load_lds_dwordx4 v[224:225], off
	v_mfma_f32_16x16x32_f16 v[78:81], v[90:93], v[134:137], v[78:81]
	ds_read_b128 v[114:117], v160 offset:51200
	v_mfma_f32_16x16x32_f16 v[22:25], v[90:93], v[138:141], v[22:25]
	ds_read_b128 v[118:121], v160 offset:53248
	v_mfma_f32_16x16x32_f16 v[30:33], v[90:93], v[142:145], v[30:33]
	s_add_u32 m0, s11, 0xa000
	ds_read_b128 v[122:125], v160 offset:55296
	global_load_lds_dwordx4 v[228:229], off
	v_mfma_f32_16x16x32_f16 v[74:77], v[94:97], v[134:137], v[74:77]
	ds_read_b128 v[126:129], v160 offset:57344
	v_mfma_f32_16x16x32_f16 v[18:21], v[94:97], v[138:141], v[18:21]
	ds_read_b128 v[130:133], v160 offset:59392
	v_mfma_f32_16x16x32_f16 v[26:29], v[94:97], v[142:145], v[26:29]
	v_mfma_f32_16x16x32_f16 v[70:73], v[98:101], v[134:137], v[70:73]
	v_mfma_f32_16x16x32_f16 v[46:49], v[98:101], v[138:141], v[46:49]
	v_mfma_f32_16x16x32_f16 v[240:243], v[98:101], v[142:145], v[240:243]
	v_mfma_f32_16x16x32_f16 v[66:69], v[102:105], v[134:137], v[66:69]
	v_mfma_f32_16x16x32_f16 v[42:45], v[102:105], v[138:141], v[42:45]
	v_mfma_f32_16x16x32_f16 v[236:239], v[102:105], v[142:145], v[236:239]
	v_mfma_f32_16x16x32_f16 v[62:65], v[106:109], v[134:137], v[62:65]
	v_mfma_f32_16x16x32_f16 v[38:41], v[106:109], v[138:141], v[38:41]
	v_mfma_f32_16x16x32_f16 v[34:37], v[106:109], v[142:145], v[34:37]
	s_waitcnt vmcnt(6) lgkmcnt(0)
	s_barrier
	s_lshl_b32 s26, s17, 2
	s_add_u32 s26, s24, s26
	s_addc_u32 s27, s25, 0
	v_lshlrev_b32_e32 v50, 2, v1
	global_load_dword v234, v50, s[26:27]
	global_load_dword v232, v50, s[26:27] offset:64
	global_load_dword v230, v50, s[26:27] offset:128
	ds_read_b128 v[134:137], v163
	v_mfma_f32_16x16x32_f16 v[82:85], v[110:113], v[146:149], v[82:85]
	ds_read_b128 v[138:141], v163 offset:2048
	v_mfma_f32_16x16x32_f16 v[58:61], v[110:113], v[150:153], v[58:61]
	ds_read_b128 v[142:145], v163 offset:4096
	v_mfma_f32_16x16x32_f16 v[14:17], v[110:113], v[154:157], v[14:17]
	ds_read_b128 v[86:89], v159
	v_mfma_f32_16x16x32_f16 v[78:81], v[114:117], v[146:149], v[78:81]
	ds_read_b128 v[90:93], v159 offset:2048
	v_mfma_f32_16x16x32_f16 v[22:25], v[114:117], v[150:153], v[22:25]
	ds_read_b128 v[94:97], v159 offset:4096
	v_mfma_f32_16x16x32_f16 v[30:33], v[114:117], v[154:157], v[30:33]
	ds_read_b128 v[98:101], v159 offset:6144
	v_mfma_f32_16x16x32_f16 v[74:77], v[118:121], v[146:149], v[74:77]
	ds_read_b128 v[102:105], v159 offset:8192
	v_mfma_f32_16x16x32_f16 v[18:21], v[118:121], v[150:153], v[18:21]
	ds_read_b128 v[106:109], v159 offset:10240
	v_mfma_f32_16x16x32_f16 v[26:29], v[118:121], v[154:157], v[26:29]
	v_mfma_f32_16x16x32_f16 v[70:73], v[122:125], v[146:149], v[70:73]
	v_mfma_f32_16x16x32_f16 v[46:49], v[122:125], v[150:153], v[46:49]
	v_mfma_f32_16x16x32_f16 v[240:243], v[122:125], v[154:157], v[240:243]
	v_mfma_f32_16x16x32_f16 v[66:69], v[126:129], v[146:149], v[66:69]
	v_mfma_f32_16x16x32_f16 v[42:45], v[126:129], v[150:153], v[42:45]
	v_mfma_f32_16x16x32_f16 v[236:239], v[126:129], v[154:157], v[236:239]
	v_mfma_f32_16x16x32_f16 v[62:65], v[130:133], v[146:149], v[62:65]
	v_mfma_f32_16x16x32_f16 v[38:41], v[130:133], v[150:153], v[38:41]
	v_mfma_f32_16x16x32_f16 v[34:37], v[130:133], v[154:157], v[34:37]
	s_waitcnt lgkmcnt(0)
	ds_read_b128 v[146:149], v165
	v_mfma_f32_16x16x32_f16 v[82:85], v[86:89], v[134:137], v[82:85]
	ds_read_b128 v[150:153], v165 offset:2048
	v_mfma_f32_16x16x32_f16 v[58:61], v[86:89], v[138:141], v[58:61]
	ds_read_b128 v[154:157], v165 offset:4096
	v_mfma_f32_16x16x32_f16 v[14:17], v[86:89], v[142:145], v[14:17]
	ds_read_b128 v[110:113], v161
	v_mfma_f32_16x16x32_f16 v[78:81], v[90:93], v[134:137], v[78:81]
	ds_read_b128 v[114:117], v161 offset:2048
	v_mfma_f32_16x16x32_f16 v[22:25], v[90:93], v[138:141], v[22:25]
	ds_read_b128 v[118:121], v161 offset:4096
	v_mfma_f32_16x16x32_f16 v[30:33], v[90:93], v[142:145], v[30:33]
	ds_read_b128 v[122:125], v161 offset:6144
	v_mfma_f32_16x16x32_f16 v[74:77], v[94:97], v[134:137], v[74:77]
	ds_read_b128 v[126:129], v161 offset:8192
	v_mfma_f32_16x16x32_f16 v[18:21], v[94:97], v[138:141], v[18:21]
	ds_read_b128 v[130:133], v161 offset:10240
	v_mfma_f32_16x16x32_f16 v[26:29], v[94:97], v[142:145], v[26:29]
	v_mfma_f32_16x16x32_f16 v[70:73], v[98:101], v[134:137], v[70:73]
	v_mfma_f32_16x16x32_f16 v[46:49], v[98:101], v[138:141], v[46:49]
	v_mfma_f32_16x16x32_f16 v[240:243], v[98:101], v[142:145], v[240:243]
	v_mfma_f32_16x16x32_f16 v[66:69], v[102:105], v[134:137], v[66:69]
	v_mfma_f32_16x16x32_f16 v[42:45], v[102:105], v[138:141], v[42:45]
	v_mfma_f32_16x16x32_f16 v[236:239], v[102:105], v[142:145], v[236:239]
	v_mfma_f32_16x16x32_f16 v[62:65], v[106:109], v[134:137], v[62:65]
	v_mfma_f32_16x16x32_f16 v[38:41], v[106:109], v[138:141], v[38:41]
	v_mfma_f32_16x16x32_f16 v[34:37], v[106:109], v[142:145], v[34:37]
	s_waitcnt vmcnt(3) lgkmcnt(0)
	s_barrier
	ds_read_b128 v[134:137], v162
	v_mfma_f32_16x16x32_f16 v[82:85], v[110:113], v[146:149], v[82:85]
	ds_read_b128 v[138:141], v162 offset:2048
	v_mfma_f32_16x16x32_f16 v[58:61], v[110:113], v[150:153], v[58:61]
	ds_read_b128 v[142:145], v162 offset:4096
	v_mfma_f32_16x16x32_f16 v[14:17], v[110:113], v[154:157], v[14:17]
	ds_read_b128 v[86:89], v158
	v_mfma_f32_16x16x32_f16 v[78:81], v[114:117], v[146:149], v[78:81]
	ds_read_b128 v[90:93], v158 offset:2048
	v_mfma_f32_16x16x32_f16 v[22:25], v[114:117], v[150:153], v[22:25]
	ds_read_b128 v[94:97], v158 offset:4096
	v_mfma_f32_16x16x32_f16 v[30:33], v[114:117], v[154:157], v[30:33]
	ds_read_b128 v[98:101], v158 offset:6144
	v_mfma_f32_16x16x32_f16 v[74:77], v[118:121], v[146:149], v[74:77]
	ds_read_b128 v[102:105], v158 offset:8192
	v_mfma_f32_16x16x32_f16 v[18:21], v[118:121], v[150:153], v[18:21]
	ds_read_b128 v[106:109], v158 offset:10240
	v_mfma_f32_16x16x32_f16 v[26:29], v[118:121], v[154:157], v[26:29]
	v_mfma_f32_16x16x32_f16 v[70:73], v[122:125], v[146:149], v[70:73]
	v_mfma_f32_16x16x32_f16 v[46:49], v[122:125], v[150:153], v[46:49]
	v_mfma_f32_16x16x32_f16 v[240:243], v[122:125], v[154:157], v[240:243]
	v_mfma_f32_16x16x32_f16 v[66:69], v[126:129], v[146:149], v[66:69]
	v_mfma_f32_16x16x32_f16 v[42:45], v[126:129], v[150:153], v[42:45]
	v_mfma_f32_16x16x32_f16 v[236:239], v[126:129], v[154:157], v[236:239]
	v_mfma_f32_16x16x32_f16 v[62:65], v[130:133], v[146:149], v[62:65]
	v_mfma_f32_16x16x32_f16 v[38:41], v[130:133], v[150:153], v[38:41]
	v_mfma_f32_16x16x32_f16 v[34:37], v[130:133], v[154:157], v[34:37]
	s_waitcnt lgkmcnt(0)
	ds_read_b128 v[146:149], v164
	v_mfma_f32_16x16x32_f16 v[82:85], v[86:89], v[134:137], v[82:85]
	ds_read_b128 v[150:153], v164 offset:2048
	v_mfma_f32_16x16x32_f16 v[58:61], v[86:89], v[138:141], v[58:61]
	ds_read_b128 v[154:157], v164 offset:4096
	v_mfma_f32_16x16x32_f16 v[14:17], v[86:89], v[142:145], v[14:17]
	ds_read_b128 v[110:113], v160
	v_mfma_f32_16x16x32_f16 v[78:81], v[90:93], v[134:137], v[78:81]
	ds_read_b128 v[114:117], v160 offset:2048
	v_mfma_f32_16x16x32_f16 v[22:25], v[90:93], v[138:141], v[22:25]
	ds_read_b128 v[118:121], v160 offset:4096
	v_mfma_f32_16x16x32_f16 v[30:33], v[90:93], v[142:145], v[30:33]
	ds_read_b128 v[122:125], v160 offset:6144
	v_mfma_f32_16x16x32_f16 v[74:77], v[94:97], v[134:137], v[74:77]
	ds_read_b128 v[126:129], v160 offset:8192
	v_mfma_f32_16x16x32_f16 v[18:21], v[94:97], v[138:141], v[18:21]
	ds_read_b128 v[130:133], v160 offset:10240
	v_mfma_f32_16x16x32_f16 v[26:29], v[94:97], v[142:145], v[26:29]
	v_mfma_f32_16x16x32_f16 v[70:73], v[98:101], v[134:137], v[70:73]
	v_mfma_f32_16x16x32_f16 v[46:49], v[98:101], v[138:141], v[46:49]
	v_mfma_f32_16x16x32_f16 v[240:243], v[98:101], v[142:145], v[240:243]
	v_mfma_f32_16x16x32_f16 v[66:69], v[102:105], v[134:137], v[66:69]
	v_mfma_f32_16x16x32_f16 v[42:45], v[102:105], v[138:141], v[42:45]
	v_mfma_f32_16x16x32_f16 v[236:239], v[102:105], v[142:145], v[236:239]
	v_mfma_f32_16x16x32_f16 v[62:65], v[106:109], v[134:137], v[62:65]
	v_mfma_f32_16x16x32_f16 v[38:41], v[106:109], v[138:141], v[38:41]
	v_mfma_f32_16x16x32_f16 v[34:37], v[106:109], v[142:145], v[34:37]
	s_waitcnt lgkmcnt(0)
	v_mfma_f32_16x16x32_f16 v[82:85], v[110:113], v[146:149], v[82:85]
	v_mfma_f32_16x16x32_f16 v[58:61], v[110:113], v[150:153], v[58:61]
	v_mfma_f32_16x16x32_f16 v[14:17], v[110:113], v[154:157], v[14:17]
	v_mfma_f32_16x16x32_f16 v[78:81], v[114:117], v[146:149], v[78:81]
	v_mfma_f32_16x16x32_f16 v[22:25], v[114:117], v[150:153], v[22:25]
	v_mfma_f32_16x16x32_f16 v[30:33], v[114:117], v[154:157], v[30:33]
	v_mfma_f32_16x16x32_f16 v[74:77], v[118:121], v[146:149], v[74:77]
	v_mfma_f32_16x16x32_f16 v[18:21], v[118:121], v[150:153], v[18:21]
	v_mfma_f32_16x16x32_f16 v[26:29], v[118:121], v[154:157], v[26:29]
	v_mfma_f32_16x16x32_f16 v[70:73], v[122:125], v[146:149], v[70:73]
	v_mfma_f32_16x16x32_f16 v[46:49], v[122:125], v[150:153], v[46:49]
	v_mfma_f32_16x16x32_f16 v[240:243], v[122:125], v[154:157], v[240:243]
	v_mfma_f32_16x16x32_f16 v[66:69], v[126:129], v[146:149], v[66:69]
	v_mfma_f32_16x16x32_f16 v[42:45], v[126:129], v[150:153], v[42:45]
	v_mfma_f32_16x16x32_f16 v[236:239], v[126:129], v[154:157], v[236:239]
	v_mfma_f32_16x16x32_f16 v[62:65], v[130:133], v[146:149], v[62:65]
	v_mfma_f32_16x16x32_f16 v[38:41], v[130:133], v[150:153], v[38:41]
	v_mfma_f32_16x16x32_f16 v[34:37], v[130:133], v[154:157], v[34:37]
